# add P0 LoRA weight table build with 9 loads in flight (opt15)
# baseline (speedup 1.0000x reference)
; __device__ __forceinline__ unsigned f2bf(float f) { return pk2(f, f) & 0xffffu; }
; __device__ __forceinline__ void p0_prologue(Frame& F, const Args& args) {
;     ...
;         bf16* wl = (bf16*)(ws + WS_WLORA);
;         for (int o = gt; o < LORA_N * LORA_K; o += NGT) {
;             const int n = o / LORA_K, k = o % LORA_K; float v = 0.f;
;             if (n < 1024) { if (k < 64) v = args.in[9][k * 1024 + n]; }
;             else if (n < 2048) { if (k >= 64 && k < 128) v = args.in[11][(k - 64) * 1024 + (n - 1024)]; }
;             else { if (k >= 128 && k < 288) v = args.in[12][(k - 128) * 1024 + (n - 2048)]; }
;             wl[o] = (bf16)f2bf(v);
;         }
;     }
.LBB0_18:
	s_or_b64 exec, exec, s[6:7]
	s_mov_b32 s5, 0x120000
	s_min_u32 s22, s12, 0x3d20
	s_min_i32 s20, s13, 1
	v_cmp_gt_i32_e32 vcc, s5, v6
	s_and_saveexec_b64 s[6:7], vcc
	s_cbranch_execz .LBB0_35
	s_cmpk_lg_i32 s93, 0x100
	s_cbranch_scc1 .Ld15_orig
	v_readlane_b32 s52, v253, 30
	v_readlane_b32 s53, v253, 31
	v_readlane_b32 s54, v253, 34
	v_readlane_b32 s55, v253, 35
	v_readlane_b32 s56, v253, 36
	v_readlane_b32 s57, v253, 37
	s_add_u32 s8, s50, 0xe00000
	s_addc_u32 s9, s51, 0
	s_mov_b32 s19, 0x2aaaaaab
	v_mov_b32_e32 v10, s52
	v_mov_b32_e32 v11, s53
	v_mov_b32_e32 v12, s54
	v_mov_b32_e32 v13, s55
	v_mov_b32_e32 v14, s56
	v_mov_b32_e32 v15, s57
	v_mov_b32_e32 v16, 0xa0
	v_mov_b32_e32 v1, v6
	v_mul_hi_u32 v2, v1, s19
	v_lshrrev_b32_e32 v2, 6, v2
	v_mul_u32_u24_e32 v4, 0x180, v2
	v_sub_u32_e32 v4, v1, v4
	v_lshrrev_b32_e32 v5, 10, v2
	v_lshlrev_b32_e32 v8, 6, v5
	v_sub_u32_e32 v4, v4, v8
	v_and_b32_e32 v2, 0x3ff, v2
	v_cmp_eq_u32_e32 vcc, 2, v5
	v_cndmask_b32_e32 v8, 64, v16, vcc
	v_cmp_lt_u32_e32 vcc, v4, v8
	v_cndmask_b32_e64 v30, 0, 1, vcc
	v_lshl_add_u32 v4, v4, 10, v2
	v_cndmask_b32_e32 v4, 0, v4, vcc
	v_cmp_eq_u32_e32 vcc, 0, v5
	v_cndmask_b32_e32 v8, v12, v10, vcc
	v_cndmask_b32_e32 v9, v13, v11, vcc
	v_cmp_eq_u32_e32 vcc, 2, v5
	v_cndmask_b32_e32 v8, v8, v14, vcc
	v_cndmask_b32_e32 v9, v9, v15, vcc
	v_mov_b32_e32 v5, 0
	v_lshl_add_u64 v[8:9], v[4:5], 2, v[8:9]
	global_load_dword v20, v[8:9], off
	v_add_u32_e32 v1, 0x20000, v6
	v_mul_hi_u32 v2, v1, s19
	v_lshrrev_b32_e32 v2, 6, v2
	v_mul_u32_u24_e32 v4, 0x180, v2
	v_sub_u32_e32 v4, v1, v4
	v_lshrrev_b32_e32 v5, 10, v2
	v_lshlrev_b32_e32 v8, 6, v5
	v_sub_u32_e32 v4, v4, v8
	v_and_b32_e32 v2, 0x3ff, v2
	v_cmp_eq_u32_e32 vcc, 2, v5
	v_cndmask_b32_e32 v8, 64, v16, vcc
	v_cmp_lt_u32_e32 vcc, v4, v8
	v_cndmask_b32_e64 v31, 0, 1, vcc
	v_lshl_add_u32 v4, v4, 10, v2
	v_cndmask_b32_e32 v4, 0, v4, vcc
	v_cmp_eq_u32_e32 vcc, 0, v5
	v_cndmask_b32_e32 v8, v12, v10, vcc
	v_cndmask_b32_e32 v9, v13, v11, vcc
	v_cmp_eq_u32_e32 vcc, 2, v5
	v_cndmask_b32_e32 v8, v8, v14, vcc
	v_cndmask_b32_e32 v9, v9, v15, vcc
	v_mov_b32_e32 v5, 0
	v_lshl_add_u64 v[8:9], v[4:5], 2, v[8:9]
	global_load_dword v21, v[8:9], off
	v_add_u32_e32 v1, 0x40000, v6
	v_mul_hi_u32 v2, v1, s19
	v_lshrrev_b32_e32 v2, 6, v2
	v_mul_u32_u24_e32 v4, 0x180, v2
	v_sub_u32_e32 v4, v1, v4
	v_lshrrev_b32_e32 v5, 10, v2
	v_lshlrev_b32_e32 v8, 6, v5
	v_sub_u32_e32 v4, v4, v8
	v_and_b32_e32 v2, 0x3ff, v2
	v_cmp_eq_u32_e32 vcc, 2, v5
	v_cndmask_b32_e32 v8, 64, v16, vcc
	v_cmp_lt_u32_e32 vcc, v4, v8
	v_cndmask_b32_e64 v32, 0, 1, vcc
	v_lshl_add_u32 v4, v4, 10, v2
	v_cndmask_b32_e32 v4, 0, v4, vcc
	v_cmp_eq_u32_e32 vcc, 0, v5
	v_cndmask_b32_e32 v8, v12, v10, vcc
	v_cndmask_b32_e32 v9, v13, v11, vcc
	v_cmp_eq_u32_e32 vcc, 2, v5
	v_cndmask_b32_e32 v8, v8, v14, vcc
	v_cndmask_b32_e32 v9, v9, v15, vcc
	v_mov_b32_e32 v5, 0
	v_lshl_add_u64 v[8:9], v[4:5], 2, v[8:9]
	global_load_dword v22, v[8:9], off
	v_add_u32_e32 v1, 0x60000, v6
	v_mul_hi_u32 v2, v1, s19
	v_lshrrev_b32_e32 v2, 6, v2
	v_mul_u32_u24_e32 v4, 0x180, v2
	v_sub_u32_e32 v4, v1, v4
	v_lshrrev_b32_e32 v5, 10, v2
	v_lshlrev_b32_e32 v8, 6, v5
	v_sub_u32_e32 v4, v4, v8
	v_and_b32_e32 v2, 0x3ff, v2
	v_cmp_eq_u32_e32 vcc, 2, v5
	v_cndmask_b32_e32 v8, 64, v16, vcc
	v_cmp_lt_u32_e32 vcc, v4, v8
	v_cndmask_b32_e64 v33, 0, 1, vcc
	v_lshl_add_u32 v4, v4, 10, v2
	v_cndmask_b32_e32 v4, 0, v4, vcc
	v_cmp_eq_u32_e32 vcc, 0, v5
	v_cndmask_b32_e32 v8, v12, v10, vcc
	v_cndmask_b32_e32 v9, v13, v11, vcc
	v_cmp_eq_u32_e32 vcc, 2, v5
	v_cndmask_b32_e32 v8, v8, v14, vcc
	v_cndmask_b32_e32 v9, v9, v15, vcc
	v_mov_b32_e32 v5, 0
	v_lshl_add_u64 v[8:9], v[4:5], 2, v[8:9]
	global_load_dword v23, v[8:9], off
	v_add_u32_e32 v1, 0x80000, v6
	v_mul_hi_u32 v2, v1, s19
	v_lshrrev_b32_e32 v2, 6, v2
	v_mul_u32_u24_e32 v4, 0x180, v2
	v_sub_u32_e32 v4, v1, v4
	v_lshrrev_b32_e32 v5, 10, v2
	v_lshlrev_b32_e32 v8, 6, v5
	v_sub_u32_e32 v4, v4, v8
	v_and_b32_e32 v2, 0x3ff, v2
	v_cmp_eq_u32_e32 vcc, 2, v5
	v_cndmask_b32_e32 v8, 64, v16, vcc
	v_cmp_lt_u32_e32 vcc, v4, v8
	v_cndmask_b32_e64 v34, 0, 1, vcc
	v_lshl_add_u32 v4, v4, 10, v2
	v_cndmask_b32_e32 v4, 0, v4, vcc
	v_cmp_eq_u32_e32 vcc, 0, v5
	v_cndmask_b32_e32 v8, v12, v10, vcc
	v_cndmask_b32_e32 v9, v13, v11, vcc
	v_cmp_eq_u32_e32 vcc, 2, v5
	v_cndmask_b32_e32 v8, v8, v14, vcc
	v_cndmask_b32_e32 v9, v9, v15, vcc
	v_mov_b32_e32 v5, 0
	v_lshl_add_u64 v[8:9], v[4:5], 2, v[8:9]
	global_load_dword v24, v[8:9], off
	v_add_u32_e32 v1, 0xa0000, v6
	v_mul_hi_u32 v2, v1, s19
	v_lshrrev_b32_e32 v2, 6, v2
	v_mul_u32_u24_e32 v4, 0x180, v2
	v_sub_u32_e32 v4, v1, v4
	v_lshrrev_b32_e32 v5, 10, v2
	v_lshlrev_b32_e32 v8, 6, v5
	v_sub_u32_e32 v4, v4, v8
	v_and_b32_e32 v2, 0x3ff, v2
	v_cmp_eq_u32_e32 vcc, 2, v5
	v_cndmask_b32_e32 v8, 64, v16, vcc
	v_cmp_lt_u32_e32 vcc, v4, v8
	v_cndmask_b32_e64 v35, 0, 1, vcc
	v_lshl_add_u32 v4, v4, 10, v2
	v_cndmask_b32_e32 v4, 0, v4, vcc
	v_cmp_eq_u32_e32 vcc, 0, v5
	v_cndmask_b32_e32 v8, v12, v10, vcc
	v_cndmask_b32_e32 v9, v13, v11, vcc
; __device__ __forceinline__ unsigned f2bf(float f) { return pk2(f, f) & 0xffffu; }
; __device__ __forceinline__ void p0_prologue(Frame& F, const Args& args) {
;     ...
;         bf16* wl = (bf16*)(ws + WS_WLORA);
;         for (int o = gt; o < LORA_N * LORA_K; o += NGT) {
;             const int n = o / LORA_K, k = o % LORA_K; float v = 0.f;
;             if (n < 1024) { if (k < 64) v = args.in[9][k * 1024 + n]; }
;             else if (n < 2048) { if (k >= 64 && k < 128) v = args.in[11][(k - 64) * 1024 + (n - 1024)]; }
;             else { if (k >= 128 && k < 288) v = args.in[12][(k - 128) * 1024 + (n - 2048)]; }
;             wl[o] = (bf16)f2bf(v);
;         }
;     }
	v_cmp_eq_u32_e32 vcc, 2, v5
	v_cndmask_b32_e32 v8, v8, v14, vcc
	v_cndmask_b32_e32 v9, v9, v15, vcc
	v_mov_b32_e32 v5, 0
	v_lshl_add_u64 v[8:9], v[4:5], 2, v[8:9]
	global_load_dword v25, v[8:9], off
	v_add_u32_e32 v1, 0xc0000, v6
	v_mul_hi_u32 v2, v1, s19
	v_lshrrev_b32_e32 v2, 6, v2
	v_mul_u32_u24_e32 v4, 0x180, v2
	v_sub_u32_e32 v4, v1, v4
	v_lshrrev_b32_e32 v5, 10, v2
	v_lshlrev_b32_e32 v8, 6, v5
	v_sub_u32_e32 v4, v4, v8
	v_and_b32_e32 v2, 0x3ff, v2
	v_cmp_eq_u32_e32 vcc, 2, v5
	v_cndmask_b32_e32 v8, 64, v16, vcc
	v_cmp_lt_u32_e32 vcc, v4, v8
	v_cndmask_b32_e64 v36, 0, 1, vcc
	v_lshl_add_u32 v4, v4, 10, v2
	v_cndmask_b32_e32 v4, 0, v4, vcc
	v_cmp_eq_u32_e32 vcc, 0, v5
	v_cndmask_b32_e32 v8, v12, v10, vcc
	v_cndmask_b32_e32 v9, v13, v11, vcc
	v_cmp_eq_u32_e32 vcc, 2, v5
	v_cndmask_b32_e32 v8, v8, v14, vcc
	v_cndmask_b32_e32 v9, v9, v15, vcc
	v_mov_b32_e32 v5, 0
	v_lshl_add_u64 v[8:9], v[4:5], 2, v[8:9]
	global_load_dword v26, v[8:9], off
	v_add_u32_e32 v1, 0xe0000, v6
	v_mul_hi_u32 v2, v1, s19
	v_lshrrev_b32_e32 v2, 6, v2
	v_mul_u32_u24_e32 v4, 0x180, v2
	v_sub_u32_e32 v4, v1, v4
	v_lshrrev_b32_e32 v5, 10, v2
	v_lshlrev_b32_e32 v8, 6, v5
	v_sub_u32_e32 v4, v4, v8
	v_and_b32_e32 v2, 0x3ff, v2
	v_cmp_eq_u32_e32 vcc, 2, v5
	v_cndmask_b32_e32 v8, 64, v16, vcc
	v_cmp_lt_u32_e32 vcc, v4, v8
	v_cndmask_b32_e64 v37, 0, 1, vcc
	v_lshl_add_u32 v4, v4, 10, v2
	v_cndmask_b32_e32 v4, 0, v4, vcc
	v_cmp_eq_u32_e32 vcc, 0, v5
	v_cndmask_b32_e32 v8, v12, v10, vcc
	v_cndmask_b32_e32 v9, v13, v11, vcc
	v_cmp_eq_u32_e32 vcc, 2, v5
	v_cndmask_b32_e32 v8, v8, v14, vcc
	v_cndmask_b32_e32 v9, v9, v15, vcc
	v_mov_b32_e32 v5, 0
	v_lshl_add_u64 v[8:9], v[4:5], 2, v[8:9]
	global_load_dword v27, v[8:9], off
	v_add_u32_e32 v1, 0x100000, v6
	v_mul_hi_u32 v2, v1, s19
	v_lshrrev_b32_e32 v2, 6, v2
	v_mul_u32_u24_e32 v4, 0x180, v2
	v_sub_u32_e32 v4, v1, v4
	v_lshrrev_b32_e32 v5, 10, v2
	v_lshlrev_b32_e32 v8, 6, v5
	v_sub_u32_e32 v4, v4, v8
	v_and_b32_e32 v2, 0x3ff, v2
	v_cmp_eq_u32_e32 vcc, 2, v5
	v_cndmask_b32_e32 v8, 64, v16, vcc
	v_cmp_lt_u32_e32 vcc, v4, v8
	v_cndmask_b32_e64 v38, 0, 1, vcc
	v_lshl_add_u32 v4, v4, 10, v2
	v_cndmask_b32_e32 v4, 0, v4, vcc
	v_cmp_eq_u32_e32 vcc, 0, v5
	v_cndmask_b32_e32 v8, v12, v10, vcc
	v_cndmask_b32_e32 v9, v13, v11, vcc
	v_cmp_eq_u32_e32 vcc, 2, v5
	v_cndmask_b32_e32 v8, v8, v14, vcc
	v_cndmask_b32_e32 v9, v9, v15, vcc
	v_mov_b32_e32 v5, 0
	v_lshl_add_u64 v[8:9], v[4:5], 2, v[8:9]
	global_load_dword v28, v[8:9], off
	s_waitcnt vmcnt(8)
	v_cmp_ne_u32_e32 vcc, 0, v30
	v_cndmask_b32_e32 v20, 0, v20, vcc
	v_cvt_pk_bf16_f32 v20, v20, v20
	v_mov_b32_e32 v4, v6
	v_mov_b32_e32 v5, 0
	v_lshl_add_u64 v[8:9], v[4:5], 1, s[8:9]
	global_store_short v[8:9], v20, off
	s_waitcnt vmcnt(7)
	v_cmp_ne_u32_e32 vcc, 0, v31
	v_cndmask_b32_e32 v21, 0, v21, vcc
	v_cvt_pk_bf16_f32 v21, v21, v21
	v_add_u32_e32 v4, 0x20000, v6
	v_mov_b32_e32 v5, 0
	v_lshl_add_u64 v[8:9], v[4:5], 1, s[8:9]
	global_store_short v[8:9], v21, off
	s_waitcnt vmcnt(6)
	v_cmp_ne_u32_e32 vcc, 0, v32
	v_cndmask_b32_e32 v22, 0, v22, vcc
	v_cvt_pk_bf16_f32 v22, v22, v22
	v_add_u32_e32 v4, 0x40000, v6
	v_mov_b32_e32 v5, 0
	v_lshl_add_u64 v[8:9], v[4:5], 1, s[8:9]
	global_store_short v[8:9], v22, off
	s_waitcnt vmcnt(5)
	v_cmp_ne_u32_e32 vcc, 0, v33
	v_cndmask_b32_e32 v23, 0, v23, vcc
	v_cvt_pk_bf16_f32 v23, v23, v23
	v_add_u32_e32 v4, 0x60000, v6
	v_mov_b32_e32 v5, 0
	v_lshl_add_u64 v[8:9], v[4:5], 1, s[8:9]
	global_store_short v[8:9], v23, off
	s_waitcnt vmcnt(4)
	v_cmp_ne_u32_e32 vcc, 0, v34
	v_cndmask_b32_e32 v24, 0, v24, vcc
	v_cvt_pk_bf16_f32 v24, v24, v24
	v_add_u32_e32 v4, 0x80000, v6
	v_mov_b32_e32 v5, 0
	v_lshl_add_u64 v[8:9], v[4:5], 1, s[8:9]
	global_store_short v[8:9], v24, off
	s_waitcnt vmcnt(3)
	v_cmp_ne_u32_e32 vcc, 0, v35
	v_cndmask_b32_e32 v25, 0, v25, vcc
	v_cvt_pk_bf16_f32 v25, v25, v25
	v_add_u32_e32 v4, 0xa0000, v6
	v_mov_b32_e32 v5, 0
	v_lshl_add_u64 v[8:9], v[4:5], 1, s[8:9]
	global_store_short v[8:9], v25, off
	s_waitcnt vmcnt(2)
	v_cmp_ne_u32_e32 vcc, 0, v36
	v_cndmask_b32_e32 v26, 0, v26, vcc
	v_cvt_pk_bf16_f32 v26, v26, v26
	v_add_u32_e32 v4, 0xc0000, v6
	v_mov_b32_e32 v5, 0
	v_lshl_add_u64 v[8:9], v[4:5], 1, s[8:9]
	global_store_short v[8:9], v26, off
	s_waitcnt vmcnt(1)
	v_cmp_ne_u32_e32 vcc, 0, v37
	v_cndmask_b32_e32 v27, 0, v27, vcc
	v_cvt_pk_bf16_f32 v27, v27, v27
	v_add_u32_e32 v4, 0xe0000, v6
	v_mov_b32_e32 v5, 0
	v_lshl_add_u64 v[8:9], v[4:5], 1, s[8:9]
	global_store_short v[8:9], v27, off
	s_waitcnt vmcnt(0)
	v_cmp_ne_u32_e32 vcc, 0, v38
	v_cndmask_b32_e32 v28, 0, v28, vcc
	v_cvt_pk_bf16_f32 v28, v28, v28
	v_add_u32_e32 v4, 0x100000, v6
	v_mov_b32_e32 v5, 0
	v_lshl_add_u64 v[8:9], v[4:5], 1, s[8:9]
	global_store_short v[8:9], v28, off
	s_branch .LBB0_35
.Ld15_orig:
	s_add_u32 s8, s50, 0xe00000
	s_addc_u32 s9, s51, 0
	v_lshlrev_b32_e32 v1, 10, v6
	s_lshl_b32 s5, s4, 10
	s_mov_b64 s[10:11], 0
	s_movk_i32 s19, 0xa0
	v_mov_b32_e32 v3, 0
	s_mov_b32 s23, 0x11ffff
	v_mov_b32_e32 v4, v6
	s_branch .LBB0_22
